# mixer C loop: the per-tile K/V LDS-DMA issue moved from right after the barrier into the MFMA stream (after the second score product)
# speedup vs baseline: 1.0026x; 1.0026x over previous
.LBB0_791:
	s_and_b32 s16, s15, 0x7000
	v_add_u32_e32 v114, s16, v249
	ds_read_b128 v[162:165], v114 offset:32768
	ds_read_b128 v[170:173], v114 offset:33280
	ds_read_b128 v[166:169], v114 offset:33792
	ds_read_b128 v[174:177], v114 offset:34304
	v_mfma_scale_f32_32x32x64_f8f6f4 v[114:129], v[198:203], v[186:191], v[2:17], v251, v250 op_sel_hi:[0,0,0] cbsz:2 blgp:2
	s_nop 0
	v_cvt_pknorm_u16_f32 v98, v98, v99
	v_cvt_pknorm_u16_f32 v99, v100, v101
	v_cvt_pknorm_u16_f32 v82, v82, v83
	v_cvt_pknorm_u16_f32 v83, v84, v85
	v_perm_b32 v178, v99, v98, s86
	v_perm_b32 v182, v83, v82, s86
	s_waitcnt lgkmcnt(4)
	v_mfma_scale_f32_32x32x64_f8f6f4 v[130:145], v[204:209], v[186:191], v[2:17], v251, v250 op_sel_hi:[0,0,0] cbsz:2 blgp:2
	s_cmp_eq_u32 s14, 0
	s_cbranch_scc1 .Lc_dma_done
	s_and_b64 vcc, exec, s[12:13]
	s_cbranch_vccz .Lc_dma_k
	s_add_i32 s4, s14, 7
	s_min_i32 s4, s4, s20
	s_lshl_b32 s58, s4, 6
	v_lshl_add_u64 v[84:85], v[226:227], 0, s[58:59]
	s_add_i32 s4, s15, 0xfffff000
	s_and_b32 s4, s4, 0x7000
	s_add_i32 s4, s4, s42
	s_mov_b32 s5, m0
	s_mov_b32 m0, s4
	s_nop 0
	global_load_lds_dwordx4 v[84:85], off
	s_mov_b32 m0, s5
	s_branch .Lc_dma_done
.Lc_dma_k:
	s_add_i32 s4, s14, 9
	s_min_i32 s4, s4, s20
	s_lshl_b32 s58, s4, 15
	v_lshl_add_u64 v[84:85], v[228:229], 0, s[58:59]
	s_add_i32 s4, s15, 0x1000
	s_and_b32 s4, s4, 0x7000
	s_add_i32 s4, s4, s41
	s_mov_b32 s5, m0
	s_mov_b32 m0, s4
	s_nop 0
	global_load_lds_dwordx4 v[84:85], off
	s_mov_b32 m0, s5
.Lc_dma_done:
	v_cvt_pknorm_u16_f32 v82, v102, v103
	v_cvt_pknorm_u16_f32 v83, v104, v105
	v_perm_b32 v179, v83, v82, s86
	v_cvt_pknorm_u16_f32 v82, v86, v87
	v_cvt_pknorm_u16_f32 v83, v88, v89
	v_perm_b32 v183, v83, v82, s86
	s_waitcnt lgkmcnt(1)
	v_mfma_scale_f32_32x32x64_f8f6f4 v[34:49], v[146:153], v[162:169], v[34:49], v248, v248 op_sel_hi:[0,0,0]
	v_cvt_pknorm_u16_f32 v82, v106, v107
	v_cvt_pknorm_u16_f32 v83, v108, v109
	v_perm_b32 v180, v83, v82, s86
	v_cvt_pknorm_u16_f32 v82, v90, v91
	v_cvt_pknorm_u16_f32 v83, v92, v93
	v_perm_b32 v184, v83, v82, s86
	s_waitcnt lgkmcnt(0)
	v_mfma_scale_f32_32x32x64_f8f6f4 v[18:33], v[146:153], v[170:177], v[18:33], v248, v248 op_sel_hi:[0,0,0]
	v_cvt_pknorm_u16_f32 v82, v110, v111
	v_cvt_pknorm_u16_f32 v83, v112, v113
	v_perm_b32 v181, v83, v82, s86
	v_cvt_pknorm_u16_f32 v82, v94, v95
	v_cvt_pknorm_u16_f32 v83, v96, v97
	v_perm_b32 v185, v83, v82, s86
	v_mfma_scale_f32_16x16x128_f8f6f4 v[210:213], v[146:153], v[154:161], v[210:213], v248, v248 op_sel_hi:[0,0,0]
	v_mfma_scale_f32_32x32x64_f8f6f4 v[98:113], v[198:203], v[192:197], v[2:17], v251, v250 op_sel_hi:[0,0,0] cbsz:2 blgp:2
	v_mfma_scale_f32_32x32x64_f8f6f4 v[82:97], v[204:209], v[192:197], v[2:17], v251, v250 op_sel_hi:[0,0,0] cbsz:2 blgp:2
	s_nop 0
	v_cvt_pknorm_u16_f32 v114, v114, v115
	v_cvt_pknorm_u16_f32 v115, v116, v117
	v_perm_b32 v146, v115, v114, s86
	v_cvt_pknorm_u16_f32 v114, v130, v131
	v_cvt_pknorm_u16_f32 v115, v132, v133
	v_perm_b32 v150, v115, v114, s86
	v_mfma_scale_f32_32x32x64_f8f6f4 v[66:81], v[178:185], v[162:169], v[66:81], v248, v248 op_sel_hi:[0,0,0]
	s_add_i32 s4, s15, 0xffffa000
	s_and_b32 s17, s4, 0x7000
	v_add_u32_e32 v130, s17, v249
	ds_read_b128 v[198:201], v130
	ds_read_b64 v[202:203], v130 offset:1024
	ds_read_b128 v[204:207], v130 offset:512
	ds_read_b64 v[208:209], v130 offset:1536
	v_cvt_pknorm_u16_f32 v118, v118, v119
	v_cvt_pknorm_u16_f32 v119, v120, v121
	v_perm_b32 v147, v119, v118, s86
	v_cvt_pknorm_u16_f32 v118, v134, v135
	v_cvt_pknorm_u16_f32 v119, v136, v137
	v_perm_b32 v151, v119, v118, s86
	v_cvt_pknorm_u16_f32 v118, v122, v123
	v_cvt_pknorm_u16_f32 v119, v124, v125
	v_perm_b32 v148, v119, v118, s86
	v_cvt_pknorm_u16_f32 v118, v138, v139
	v_cvt_pknorm_u16_f32 v119, v140, v141
	v_perm_b32 v152, v119, v118, s86
	v_mfma_scale_f32_32x32x64_f8f6f4 v[50:65], v[178:185], v[170:177], v[50:65], v248, v248 op_sel_hi:[0,0,0]
	v_cvt_pknorm_u16_f32 v118, v126, v127
	v_cvt_pknorm_u16_f32 v119, v128, v129
	v_perm_b32 v149, v119, v118, s86
	v_cvt_pknorm_u16_f32 v118, v142, v143
	v_cvt_pknorm_u16_f32 v119, v144, v145
	v_perm_b32 v153, v119, v118, s86
	v_mfma_scale_f32_16x16x128_f8f6f4 v[214:217], v[178:185], v[154:161], v[214:217], v248, v248 op_sel_hi:[0,0,0]
	s_waitcnt vmcnt(6) lgkmcnt(0)
	s_barrier
	s_branch .LBB0_790
